# v39 shifted by 32 bytes (eight s_nop at the entry): code placement scan
# speedup vs baseline: 1.0026x; 1.0009x over previous
_Z10hybrid_fwd4Args:
	s_nop 0
	s_nop 0
	s_nop 0
	s_nop 0
	s_nop 0
	s_nop 0
	s_nop 0
	s_nop 0
	s_mov_b32 s99, 0
	s_load_dwordx2 s[78:79], s[0:1], 0xb0
	s_load_dwordx4 s[4:7], s[0:1], 0xa0
	s_mov_b32 s74, s2
	s_add_u32 s2, s0, 0xc0
	s_addc_u32 s3, s1, 0
	v_readfirstlane_b32 s64, v0
	s_waitcnt lgkmcnt(0)
	v_writelane_b32 v254, s4, 0
	s_mov_b32 s71, s74
	s_nop 0
	v_writelane_b32 v254, s5, 1
	v_writelane_b32 v254, s6, 2
	v_writelane_b32 v254, s7, 3
	s_load_dword s80, s[0:1], 0xc0
	s_load_dwordx8 s[4:11], s[0:1], 0x80
	s_waitcnt lgkmcnt(0)
	v_writelane_b32 v254, s4, 4
	s_nop 1
	v_writelane_b32 v254, s5, 5
	v_writelane_b32 v254, s6, 6
	v_writelane_b32 v254, s7, 7
	v_writelane_b32 v254, s8, 8
	v_writelane_b32 v254, s9, 9
	v_writelane_b32 v254, s10, 10
	v_writelane_b32 v254, s11, 11
	v_writelane_b32 v254, s2, 12
	s_nop 1
	v_writelane_b32 v254, s3, 13
	s_and_b32 s2, s80, 7
	s_cmp_lg_u32 s2, 0
	s_cbranch_scc0 .LBB0_42
	s_load_dwordx2 s[96:97], s[0:1], 0xb8
	v_cmp_gt_u32_e32 vcc, 4, v0
	s_and_saveexec_b64 s[4:5], vcc
